# fused MoE K-loop: first iteration after a gate/up epilogue (16 stores) uses vmcnt(24)/vmcnt(10) so the restart does not wait for the epilogue stores; plus previous changes
# baseline (speedup 1.0000x reference)
;     __device__ __forceinline__ bf16_t* gu() const { return (bf16_t*)(ws + WS_GU); }
;     __device__ __forceinline__ bf16_t* dn() const { return (bf16_t*)(ws + WS_DN); }
;     __device__ __forceinline__ bf16_t* H() const { return (bf16_t*)(ws + WS_H); }
;     __device__ __forceinline__ int* rtok() const { return (int*)(ws + WS_RTOK); }
;     __device__ __forceinline__ float* rw() const { return (float*)(ws + WS_RW); }
;     __device__ __forceinline__ bf16_t* Y() const { return (bf16_t*)(ws + WS_Y); }
;     __device__ __forceinline__ bf16_t* acts() const { return (bf16_t*)(ws + WS_ACTS); }
; __device__ __forceinline__ LAS int* moe_tb(const Frame& F) { return (LAS int*)(F.lds + LDS_MISC + 64); }
; #define PB_BEGIN(id) unsigned long long _pt0_##id = (((PROBE_MASK) >> (id)) & 1) ? __builtin_amdgcn_s_memrealtime() : 0ull
; #define PB_END(id) do { if (((PROBE_MASK) >> (id)) & 1) { __syncthreads(); const unsigned long long _t1 = __builtin_amdgcn_s_memrealtime(), _w = (_t1 - _pt0_##id) * (PROBE_MUL); \
;         while (__builtin_amdgcn_s_memrealtime() - _t1 < _w) __builtin_amdgcn_s_sleep(8); } } while (0)
; #define PB_BEGIN(id) do {} while (0)
; #define PB_END(id) do {} while (0)
; __global__ void __launch_bounds__(NTHR, 2) fwd_kernel(Params prm) {
;     ...
;                 SchedMoeFused S{(const char*)F.H(), (const char*)F.gu(), (const char*)F.dn(), (const char*)F.acts(), F.rtok(), moe_tb(F), nfull, G, c, (unsigned)F.wg * (256u * 2048u)};
;                 EpiMoe E{(char*)F.acts(), prm.b_e_gate + (size_t)l * NEXP * DM, prm.b_e_up + (size_t)l * NEXP * DM, prm.b_e_down + (size_t)l * NEXP * DM, F.rtok(), F.rw(), F.Y(), true};
;                 PB_BEGIN(13); gm::gemm_phase<true>(F.lds, S, E); PB_END(13);
.LBB0_1771:
	v_readlane_b32 s30, v255, 11
	v_readlane_b32 s31, v255, 12
	s_add_u32 s58, s30, 0xb716100
	s_addc_u32 s59, s31, 0
	s_add_u32 s63, s30, 0x3d316100
	s_addc_u32 s71, s31, 0
	s_lshl_b64 s[0:1], s[0:1], 2
	v_readlane_b32 s28, v253, 26
	v_readlane_b32 s29, v253, 27
	s_add_u32 s72, s28, s0
	s_addc_u32 s73, s29, s1
	s_add_u32 s0, s30, 0x45a36100
	s_addc_u32 s1, s31, 0
	s_add_u32 s44, s30, 0x1c316100
	s_addc_u32 s45, s31, 0
	s_andn2_b64 vcc, exec, s[22:23]
	s_cbranch_vccnz .LBB0_1825
	s_mov_b32 s100, 0
	v_mov_b32_e32 v2, v0
	v_writelane_b32 v255, s80, 4
	v_ashrrev_i32_e32 v4, 31, v2
	v_lshrrev_b32_e32 v4, 26, v4
	v_lshlrev_b32_e32 v3, 4, v2
	v_add_u32_e32 v4, v2, v4
	v_bfe_i32 v2, v2, 27, 1
	v_lshrrev_b32_e32 v2, 22, v2
	v_add_u32_e32 v2, v3, v2
	v_and_b32_e32 v2, 0xfffffc00, v2
	v_sub_u32_e32 v2, v3, v2
	v_ashrrev_i32_e32 v7, 6, v4
	v_lshrrev_b32_e32 v4, 4, v2
	v_bitop3_b32 v8, v4, v2, 32 bitop3:0x6c
	v_ashrrev_i32_e32 v4, 31, v8
	v_lshrrev_b32_e32 v4, 26, v4
	v_add_u32_e32 v4, v8, v4
	v_add_u32_e32 v3, 0x2000, v3
	v_ashrrev_i32_e32 v6, 6, v4
	v_ashrrev_i32_e32 v4, 31, v3
	v_lshrrev_b32_e32 v4, 22, v4
	v_add_u32_e32 v4, v3, v4
	v_ashrrev_i32_e32 v10, 10, v4
	v_mul_i32_i24_e32 v4, 0x400, v10
	v_sub_u32_e32 v3, v3, v4
	v_lshrrev_b32_e32 v4, 4, v3
	v_bitop3_b32 v11, v4, v3, 32 bitop3:0x6c
	v_ashrrev_i32_e32 v4, 31, v11
	v_lshrrev_b32_e32 v4, 26, v4
	v_lshlrev_b32_e32 v2, 3, v7
	v_lshlrev_b32_e32 v3, 3, v10
	v_add_u32_e32 v4, v11, v4
	v_and_b32_e32 v2, -16, v2
	v_and_b32_e32 v3, -16, v3
	v_ashrrev_i32_e32 v9, 6, v4
	v_add_u32_e32 v2, v6, v2
	s_cmp_eq_u64 s[8:9], 0
	v_add_u32_e32 v4, v9, v3
	v_writelane_b32 v255, s81, 5
	s_cbranch_scc1 .LBB0_1774
	v_ashrrev_i32_e32 v3, 31, v2
	v_ashrrev_i32_e32 v5, 31, v4
	v_lshl_add_u64 v[12:13], v[2:3], 2, s[8:9]
	v_lshl_add_u64 v[14:15], v[4:5], 2, s[8:9]
	global_load_dword v3, v[12:13], off
	global_load_dword v5, v[14:15], off
	s_nop 0
	global_load_dword v14, v[14:15], off offset:512
	s_nop 0
	global_load_dword v12, v[12:13], off offset:512
	s_waitcnt vmcnt(3)
	v_max_i32_e32 v3, 0, v3
	s_waitcnt vmcnt(2)
	v_max_i32_e32 v5, 0, v5
	s_waitcnt vmcnt(1)
	v_max_i32_e32 v14, 0, v14
	s_waitcnt vmcnt(0)
	v_max_i32_e32 v15, 0, v12
	v_lshrrev_b32_e32 v13, 2, v3
	v_lshrrev_b32_e32 v12, 2, v5
	v_lshrrev_b32_e32 v3, 2, v15
	v_lshrrev_b32_e32 v5, 2, v14
	s_branch .LBB0_1775

; #define G_STAGE2(bufoff, gbase, v0, v1) do { \
;         __builtin_amdgcn_global_load_lds((const unsigned*)((const char*)(gbase) + (v0)), (LAS unsigned*)(lds + (bufoff) + ldsw), 16, 0, 0); \
;         __builtin_amdgcn_global_load_lds((const unsigned*)((const char*)(gbase) + (v1)), (LAS unsigned*)(lds + (bufoff) + ldsw + 8192), 16, 0, 0); } while (0)
; #define G_LDA(dst, b, h) do { _Pragma("unroll") for (int m = 0; m < 4; ++m) _Pragma("unroll") for (int k = 0; k < 2; ++k) dst[m][k] = *(const LAS bf16x8*)(lds + G_SA(b, h) + aoff + m * 2048 + k * 1024); } while (0)
; #define G_LDB(dst, b, h) do { _Pragma("unroll") for (int n = 0; n < 2; ++n) _Pragma("unroll") for (int k = 0; k < 2; ++k) dst[n][k] = *(const LAS bf16x8*)(lds + G_SB(b, h) + boff + n * 2048 + k * 1024); } while (0)
; #define G_MMA(ai, bj, At, Bt) do { __builtin_amdgcn_s_setprio(1); _Pragma("unroll") for (int m = 0; m < 4; ++m) _Pragma("unroll") for (int n = 0; n < 2; ++n) _Pragma("unroll") for (int k = 0; k < 2; ++k) \
;         acc[ai][bj][m][n] = __builtin_amdgcn_mfma_f32_16x16x32_bf16(Bt[n][k], At[m][k], acc[ai][bj][m][n], 0, 0, 0); __builtin_amdgcn_s_setprio(0); } while (0)
; #define G_WAIT_V(n) asm volatile("s_waitcnt vmcnt(" #n ")" ::: "memory")
; #define G_WAIT_L(n) asm volatile("s_waitcnt lgkmcnt(" #n ")" ::: "memory")
; #define G_BAR __builtin_amdgcn_s_barrier()
; #define G_SCHED __builtin_amdgcn_sched_barrier(0)
; template <bool PERM, class Epi, class Sched>
; __device__ __forceinline__ void gemm_phase(LAS unsigned char* lds, const Sched& S, const Epi& E) {
;     ...
;             G_WAIT_L(8); G_BAR; G_WAIT_L(0); G_MMA(0, 0, At, B0); G_BAR; G_SCHED;
;             G_LDB(B1, 0, 1); G_STAGE2(G_SB(0, 0), b2, vb0, vb1);
;             G_BAR; G_WAIT_L(0); G_MMA(0, 1, At, B1); G_BAR;
;             G_LDA(At, 0, 1); G_STAGE2(G_SA(0, 0), a2, va00, va01);
;             G_BAR; G_WAIT_L(0); G_MMA(1, 0, At, B0); G_BAR; G_SCHED;
;             G_STAGE2(G_SB(0, 1), b2 + hsB, vb0, vb1);
;             G_WAIT_V(6); G_BAR; G_MMA(1, 1, At, B1); G_BAR;
.LBB0_1797:
	s_add_u32 s18, s28, 0x80
	s_waitcnt lgkmcnt(8)
	s_barrier
	s_waitcnt lgkmcnt(0)
	s_addc_u32 s19, s29, 0
	s_and_b64 s[8:9], s[8:9], exec
	s_cselect_b32 s19, s61, s19
	s_cselect_b32 s18, s60, s18
	s_cselect_b32 s9, s55, s23
	s_cselect_b32 s8, s54, s22
	s_setprio 1
	s_waitcnt lgkmcnt(0)
	v_mfma_f32_16x16x32_bf16 v[134:137], v[122:125], v[172:175], v[134:137]
	v_mfma_f32_16x16x32_bf16 v[130:133], v[138:141], v[172:175], v[130:133]
	v_mfma_f32_16x16x32_bf16 v[118:121], v[122:125], v[164:167], v[118:121]
	v_mfma_f32_16x16x32_bf16 v[114:117], v[138:141], v[164:167], v[114:117]
	v_mfma_f32_16x16x32_bf16 v[110:113], v[122:125], v[156:159], v[110:113]
	v_mfma_f32_16x16x32_bf16 v[106:109], v[138:141], v[156:159], v[106:109]
	v_mfma_f32_16x16x32_bf16 v[102:105], v[122:125], v[148:151], v[102:105]
	v_mfma_f32_16x16x32_bf16 v[98:101], v[138:141], v[148:151], v[98:101]
	v_mfma_f32_16x16x32_bf16 v[134:137], v[126:129], v[176:179], v[134:137]
	v_mfma_f32_16x16x32_bf16 v[130:133], v[142:145], v[176:179], v[130:133]
	v_mfma_f32_16x16x32_bf16 v[118:121], v[126:129], v[168:171], v[118:121]
	v_mfma_f32_16x16x32_bf16 v[114:117], v[142:145], v[168:171], v[114:117]
	v_mfma_f32_16x16x32_bf16 v[110:113], v[126:129], v[160:163], v[110:113]
	v_mfma_f32_16x16x32_bf16 v[106:109], v[142:145], v[160:163], v[106:109]
	v_mfma_f32_16x16x32_bf16 v[102:105], v[126:129], v[152:155], v[102:105]
	v_mfma_f32_16x16x32_bf16 v[98:101], v[142:145], v[152:155], v[98:101]
	s_setprio 0
	s_barrier
	s_add_i32 s25, 0, 0x14000
	s_mov_b32 m0, s82
	v_add_u32_e32 v181, s25, v1
	ds_read_b128 v[206:209], v181
	ds_read_b128 v[210:213], v181 offset:1024
	ds_read_b128 v[214:217], v181 offset:2048
	ds_read_b128 v[218:221], v181 offset:3072
	global_load_lds_dwordx4 v146, s[8:9]
	s_mov_b32 m0, s83
	v_mov_b32_e32 v189, v147
	global_load_lds_dwordx4 v188, s[8:9]
	s_barrier
	s_waitcnt lgkmcnt(0)
	v_lshl_add_u64 v[222:223], s[8:9], 0, v[146:147]
	v_lshl_add_u64 v[224:225], s[8:9], 0, v[188:189]
	s_setprio 1
	s_waitcnt lgkmcnt(0)
	v_mfma_f32_16x16x32_bf16 v[62:65], v[206:209], v[172:175], v[62:65]
	v_mfma_f32_16x16x32_bf16 v[58:61], v[214:217], v[172:175], v[58:61]
	v_mfma_f32_16x16x32_bf16 v[54:57], v[206:209], v[164:167], v[54:57]
	v_mfma_f32_16x16x32_bf16 v[50:53], v[214:217], v[164:167], v[50:53]
	v_mfma_f32_16x16x32_bf16 v[46:49], v[206:209], v[156:159], v[46:49]
	v_mfma_f32_16x16x32_bf16 v[42:45], v[214:217], v[156:159], v[42:45]
	v_mfma_f32_16x16x32_bf16 v[38:41], v[206:209], v[148:151], v[38:41]
	v_mfma_f32_16x16x32_bf16 v[34:37], v[214:217], v[148:151], v[34:37]
	v_mfma_f32_16x16x32_bf16 v[62:65], v[210:213], v[176:179], v[62:65]
	v_mfma_f32_16x16x32_bf16 v[58:61], v[218:221], v[176:179], v[58:61]
	v_mfma_f32_16x16x32_bf16 v[54:57], v[210:213], v[168:171], v[54:57]
	v_mfma_f32_16x16x32_bf16 v[50:53], v[218:221], v[168:171], v[50:53]
	v_mfma_f32_16x16x32_bf16 v[46:49], v[210:213], v[160:163], v[46:49]
	v_mfma_f32_16x16x32_bf16 v[42:45], v[218:221], v[160:163], v[42:45]
	v_mfma_f32_16x16x32_bf16 v[38:41], v[210:213], v[152:155], v[38:41]
	v_mfma_f32_16x16x32_bf16 v[34:37], v[218:221], v[152:155], v[34:37]
	s_setprio 0
	s_mov_b32 m0, s81
	s_barrier
	ds_read_b128 v[148:151], v199 offset:16384
	ds_read_b128 v[152:155], v199 offset:17408
	ds_read_b128 v[156:159], v199 offset:18432
	ds_read_b128 v[160:163], v199 offset:19456
	ds_read_b128 v[164:167], v199 offset:20480
	ds_read_b128 v[168:171], v199 offset:21504
	ds_read_b128 v[172:175], v199 offset:22528
	ds_read_b128 v[176:179], v199 offset:23552
	global_load_lds_dwordx4 v180, s[18:19]
	s_mov_b32 m0, s84
	v_mov_b32_e32 v181, v147
	global_load_lds_dwordx4 v186, s[18:19]
	s_barrier
	s_waitcnt lgkmcnt(0)
	v_mov_b32_e32 v187, v147
	v_lshl_add_u64 v[234:235], s[18:19], 0, v[180:181]
	v_lshl_add_u64 v[238:239], s[18:19], 0, v[186:187]
	s_setprio 1
	s_waitcnt lgkmcnt(0)
	v_mfma_f32_16x16x32_bf16 v[94:97], v[122:125], v[148:151], v[94:97]
	v_mfma_f32_16x16x32_bf16 v[90:93], v[138:141], v[148:151], v[90:93]
	v_mfma_f32_16x16x32_bf16 v[86:89], v[122:125], v[156:159], v[86:89]
	v_mfma_f32_16x16x32_bf16 v[82:85], v[138:141], v[156:159], v[82:85]
	v_mfma_f32_16x16x32_bf16 v[78:81], v[122:125], v[164:167], v[78:81]
	v_mfma_f32_16x16x32_bf16 v[74:77], v[138:141], v[164:167], v[74:77]
	v_mfma_f32_16x16x32_bf16 v[70:73], v[122:125], v[172:175], v[70:73]
	v_mfma_f32_16x16x32_bf16 v[66:69], v[138:141], v[172:175], v[66:69]
	v_mfma_f32_16x16x32_bf16 v[94:97], v[126:129], v[152:155], v[94:97]
	v_mfma_f32_16x16x32_bf16 v[90:93], v[142:145], v[152:155], v[90:93]
	v_mfma_f32_16x16x32_bf16 v[86:89], v[126:129], v[160:163], v[86:89]
	v_mfma_f32_16x16x32_bf16 v[82:85], v[142:145], v[160:163], v[82:85]
	v_mfma_f32_16x16x32_bf16 v[78:81], v[126:129], v[168:171], v[78:81]
	v_mfma_f32_16x16x32_bf16 v[74:77], v[142:145], v[168:171], v[74:77]
	v_mfma_f32_16x16x32_bf16 v[70:73], v[126:129], v[176:179], v[70:73]
	v_mfma_f32_16x16x32_bf16 v[66:69], v[142:145], v[176:179], v[66:69]
	s_setprio 0
	s_barrier
	s_add_u32 vcc_lo, s8, 0x40000
	s_addc_u32 vcc_hi, s9, 0
	s_add_i32 s25, s25, s80
	s_mov_b32 m0, s25
	s_nop 0
	global_load_lds_dwordx4 v146, vcc
	s_add_i32 m0, s25, 0x2000
	s_nop 0
	global_load_lds_dwordx4 v188, vcc
	s_cmp_lg_u32 s100, 0
	s_cbranch_scc1 .Lmf_p4s
	s_waitcnt vmcnt(6)
	s_branch .Lmf_p4j

; #define G_STAGE2(bufoff, gbase, v0, v1) do { \
;         __builtin_amdgcn_global_load_lds((const unsigned*)((const char*)(gbase) + (v0)), (LAS unsigned*)(lds + (bufoff) + ldsw), 16, 0, 0); \
;         __builtin_amdgcn_global_load_lds((const unsigned*)((const char*)(gbase) + (v1)), (LAS unsigned*)(lds + (bufoff) + ldsw + 8192), 16, 0, 0); } while (0)
; #define G_LDA(dst, b, h) do { _Pragma("unroll") for (int m = 0; m < 4; ++m) _Pragma("unroll") for (int k = 0; k < 2; ++k) dst[m][k] = *(const LAS bf16x8*)(lds + G_SA(b, h) + aoff + m * 2048 + k * 1024); } while (0)
; #define G_LDB(dst, b, h) do { _Pragma("unroll") for (int n = 0; n < 2; ++n) _Pragma("unroll") for (int k = 0; k < 2; ++k) dst[n][k] = *(const LAS bf16x8*)(lds + G_SB(b, h) + boff + n * 2048 + k * 1024); } while (0)
; #define G_MMA(ai, bj, At, Bt) do { __builtin_amdgcn_s_setprio(1); _Pragma("unroll") for (int m = 0; m < 4; ++m) _Pragma("unroll") for (int n = 0; n < 2; ++n) _Pragma("unroll") for (int k = 0; k < 2; ++k) \
;         acc[ai][bj][m][n] = __builtin_amdgcn_mfma_f32_16x16x32_bf16(Bt[n][k], At[m][k], acc[ai][bj][m][n], 0, 0, 0); __builtin_amdgcn_s_setprio(0); } while (0)
; #define G_WAIT_V(n) asm volatile("s_waitcnt vmcnt(" #n ")" ::: "memory")
; #define G_WAIT_L(n) asm volatile("s_waitcnt lgkmcnt(" #n ")" ::: "memory")
; #define G_BAR __builtin_amdgcn_s_barrier()
; #define G_SCHED __builtin_amdgcn_sched_barrier(0)
; template <bool PERM, class Epi, class Sched>
; __device__ __forceinline__ void gemm_phase(LAS unsigned char* lds, const Sched& S, const Epi& E) {
;     ...
;             G_WAIT_V(6); G_BAR; G_MMA(1, 1, At, B1); G_BAR;
;             G_LDB(B0, 1, 0); G_SCHED; G_LDA(At, 1, 0); G_STAGE2(G_SA(0, 1), a2, va10, va11);
;             G_WAIT_L(8); G_BAR; G_WAIT_L(0); G_MMA(0, 0, At, B0); G_BAR; G_SCHED;
;             G_LDB(B1, 1, 1); G_STAGE2(G_SB(1, 0), b3, vb0, vb1);
;             G_BAR; G_WAIT_L(0); G_MMA(0, 1, At, B1); G_BAR;
.Lmf_p4j:
	s_barrier
	s_setprio 1
	v_mfma_f32_16x16x32_bf16 v[30:33], v[206:209], v[148:151], v[30:33]
	v_mfma_f32_16x16x32_bf16 v[26:29], v[214:217], v[148:151], v[26:29]
	v_mfma_f32_16x16x32_bf16 v[22:25], v[206:209], v[156:159], v[22:25]
	v_mfma_f32_16x16x32_bf16 v[18:21], v[214:217], v[156:159], v[18:21]
	v_mfma_f32_16x16x32_bf16 v[14:17], v[206:209], v[164:167], v[14:17]
	v_mfma_f32_16x16x32_bf16 v[10:13], v[214:217], v[164:167], v[10:13]
	v_mfma_f32_16x16x32_bf16 v[6:9], v[206:209], v[172:175], v[6:9]
	v_mfma_f32_16x16x32_bf16 v[2:5], v[214:217], v[172:175], v[2:5]
	v_mfma_f32_16x16x32_bf16 v[30:33], v[210:213], v[152:155], v[30:33]
	v_mfma_f32_16x16x32_bf16 v[26:29], v[218:221], v[152:155], v[26:29]
	v_mfma_f32_16x16x32_bf16 v[22:25], v[210:213], v[160:163], v[22:25]
	v_mfma_f32_16x16x32_bf16 v[18:21], v[218:221], v[160:163], v[18:21]
	v_mfma_f32_16x16x32_bf16 v[14:17], v[210:213], v[168:171], v[14:17]
	v_mfma_f32_16x16x32_bf16 v[10:13], v[218:221], v[168:171], v[10:13]
	v_mfma_f32_16x16x32_bf16 v[6:9], v[210:213], v[176:179], v[6:9]
	v_mfma_f32_16x16x32_bf16 v[2:5], v[218:221], v[176:179], v[2:5]
	s_setprio 0
	s_add_i32 s25, 0, 0x18000
	v_add_u32_e32 v142, s25, v1
	s_barrier
	ds_read_b128 v[122:125], v142
	ds_read_b128 v[126:129], v142 offset:1024
	ds_read_b128 v[138:141], v142 offset:2048
	ds_read_b128 v[142:145], v142 offset:3072
	s_mov_b32 m0, s85
	v_lshl_add_u64 v[200:201], s[18:19], 0, v[200:201]
	ds_read_b128 v[148:151], v199 offset:32768
	ds_read_b128 v[152:155], v199 offset:33792
	ds_read_b128 v[156:159], v199 offset:34816
	ds_read_b128 v[160:163], v199 offset:35840
	ds_read_b128 v[164:167], v199 offset:36864
	ds_read_b128 v[168:171], v199 offset:37888
	ds_read_b128 v[172:175], v199 offset:38912
	ds_read_b128 v[176:179], v199 offset:39936
	global_load_lds_dwordx4 v[200:201], off
	v_lshl_add_u64 v[194:195], s[18:19], 0, v[194:195]
	s_mov_b32 m0, s86
	s_nop 0
	global_load_lds_dwordx4 v[194:195], off
	s_waitcnt lgkmcnt(8)
	s_barrier
	s_waitcnt lgkmcnt(0)
	s_setprio 1
	s_waitcnt lgkmcnt(0)
	v_mfma_f32_16x16x32_bf16 v[134:137], v[122:125], v[148:151], v[134:137]
	v_mfma_f32_16x16x32_bf16 v[130:133], v[138:141], v[148:151], v[130:133]
	v_mfma_f32_16x16x32_bf16 v[118:121], v[122:125], v[156:159], v[118:121]
	v_mfma_f32_16x16x32_bf16 v[114:117], v[138:141], v[156:159], v[114:117]
	v_mfma_f32_16x16x32_bf16 v[110:113], v[122:125], v[164:167], v[110:113]
	v_mfma_f32_16x16x32_bf16 v[106:109], v[138:141], v[164:167], v[106:109]
	v_mfma_f32_16x16x32_bf16 v[102:105], v[122:125], v[172:175], v[102:105]
	v_mfma_f32_16x16x32_bf16 v[98:101], v[138:141], v[172:175], v[98:101]
	v_mfma_f32_16x16x32_bf16 v[134:137], v[126:129], v[152:155], v[134:137]
	v_mfma_f32_16x16x32_bf16 v[130:133], v[142:145], v[152:155], v[130:133]
	v_mfma_f32_16x16x32_bf16 v[118:121], v[126:129], v[160:163], v[118:121]
	v_mfma_f32_16x16x32_bf16 v[114:117], v[142:145], v[160:163], v[114:117]
	v_mfma_f32_16x16x32_bf16 v[110:113], v[126:129], v[168:171], v[110:113]
	v_mfma_f32_16x16x32_bf16 v[106:109], v[142:145], v[168:171], v[106:109]
	v_mfma_f32_16x16x32_bf16 v[102:105], v[126:129], v[176:179], v[102:105]
	v_mfma_f32_16x16x32_bf16 v[98:101], v[142:145], v[176:179], v[98:101]
	s_setprio 0
	s_barrier
	s_add_i32 s18, 0, 0x1c000
	s_add_i32 s19, s25, s80
	v_add_u32_e32 v181, s18, v1
	v_lshl_add_u64 v[194:195], v[222:223], 0, s[34:35]
	s_mov_b32 m0, s19
	ds_read_b128 v[206:209], v181
	ds_read_b128 v[210:213], v181 offset:1024
	ds_read_b128 v[214:217], v181 offset:2048
	ds_read_b128 v[218:221], v181 offset:3072
	global_load_lds_dwordx4 v[194:195], off
	v_lshl_add_u64 v[194:195], v[224:225], 0, s[34:35]
	s_add_i32 m0, s19, 0x2000
	s_nop 0
	global_load_lds_dwordx4 v[194:195], off
	s_cmp_eq_u32 s100, 0
	s_cbranch_scc1 .Lmf_p6n
	s_waitcnt vmcnt(10)
; #define G_STAGE2(bufoff, gbase, v0, v1) do { \
;         __builtin_amdgcn_global_load_lds((const unsigned*)((const char*)(gbase) + (v0)), (LAS unsigned*)(lds + (bufoff) + ldsw), 16, 0, 0); \
;         __builtin_amdgcn_global_load_lds((const unsigned*)((const char*)(gbase) + (v1)), (LAS unsigned*)(lds + (bufoff) + ldsw + 8192), 16, 0, 0); } while (0)
; #define G_LDA(dst, b, h) do { _Pragma("unroll") for (int m = 0; m < 4; ++m) _Pragma("unroll") for (int k = 0; k < 2; ++k) dst[m][k] = *(const LAS bf16x8*)(lds + G_SA(b, h) + aoff + m * 2048 + k * 1024); } while (0)
; #define G_MMA(ai, bj, At, Bt) do { __builtin_amdgcn_s_setprio(1); _Pragma("unroll") for (int m = 0; m < 4; ++m) _Pragma("unroll") for (int n = 0; n < 2; ++n) _Pragma("unroll") for (int k = 0; k < 2; ++k) \
;         acc[ai][bj][m][n] = __builtin_amdgcn_mfma_f32_16x16x32_bf16(Bt[n][k], At[m][k], acc[ai][bj][m][n], 0, 0, 0); __builtin_amdgcn_s_setprio(0); } while (0)
; #define G_WAIT_V(n) asm volatile("s_waitcnt vmcnt(" #n ")" ::: "memory")
; #define G_WAIT_L(n) asm volatile("s_waitcnt lgkmcnt(" #n ")" ::: "memory")
; #define G_BAR __builtin_amdgcn_s_barrier()
; #define G_SCHED __builtin_amdgcn_sched_barrier(0)
; template <bool PERM, class Epi, class Sched>
; __device__ __forceinline__ void gemm_phase(LAS unsigned char* lds, const Sched& S, const Epi& E) {
;     ...
;             G_BAR; G_WAIT_L(0); G_MMA(0, 1, At, B1); G_BAR;
;             G_LDA(At, 1, 1); G_STAGE2(G_SA(1, 0), a3, va00, va01);
;             G_BAR; G_WAIT_L(0); G_MMA(1, 0, At, B0); G_BAR; G_SCHED;
;             G_STAGE2(G_SB(1, 1), b3 + hsB, vb0, vb1);
;             G_WAIT_V(6); G_BAR; G_MMA(1, 1, At, B1); G_BAR;
;         }
.Lmf_p6n:
	s_barrier
	s_waitcnt lgkmcnt(0)
	s_setprio 1
	s_waitcnt lgkmcnt(0)
	v_mfma_f32_16x16x32_bf16 v[62:65], v[206:209], v[148:151], v[62:65]
	v_mfma_f32_16x16x32_bf16 v[58:61], v[214:217], v[148:151], v[58:61]
	v_mfma_f32_16x16x32_bf16 v[54:57], v[206:209], v[156:159], v[54:57]
	v_mfma_f32_16x16x32_bf16 v[50:53], v[214:217], v[156:159], v[50:53]
	v_mfma_f32_16x16x32_bf16 v[46:49], v[206:209], v[164:167], v[46:49]
	v_mfma_f32_16x16x32_bf16 v[42:45], v[214:217], v[164:167], v[42:45]
	v_mfma_f32_16x16x32_bf16 v[38:41], v[206:209], v[172:175], v[38:41]
	v_mfma_f32_16x16x32_bf16 v[34:37], v[214:217], v[172:175], v[34:37]
	v_mfma_f32_16x16x32_bf16 v[62:65], v[210:213], v[152:155], v[62:65]
	v_mfma_f32_16x16x32_bf16 v[58:61], v[218:221], v[152:155], v[58:61]
	v_mfma_f32_16x16x32_bf16 v[54:57], v[210:213], v[160:163], v[54:57]
	v_mfma_f32_16x16x32_bf16 v[50:53], v[218:221], v[160:163], v[50:53]
	v_mfma_f32_16x16x32_bf16 v[46:49], v[210:213], v[168:171], v[46:49]
	v_mfma_f32_16x16x32_bf16 v[42:45], v[218:221], v[168:171], v[42:45]
	v_mfma_f32_16x16x32_bf16 v[38:41], v[210:213], v[176:179], v[38:41]
	v_mfma_f32_16x16x32_bf16 v[34:37], v[218:221], v[176:179], v[34:37]
	s_setprio 0
	s_mov_b32 m0, s89
	v_lshl_add_u64 v[194:195], v[234:235], 0, s[34:35]
	s_barrier
	ds_read_b128 v[148:151], v199 offset:49152
	ds_read_b128 v[152:155], v199 offset:50176
	ds_read_b128 v[156:159], v199 offset:51200
	ds_read_b128 v[160:163], v199 offset:52224
	ds_read_b128 v[164:167], v199 offset:53248
	ds_read_b128 v[168:171], v199 offset:54272
	ds_read_b128 v[172:175], v199 offset:55296
	ds_read_b128 v[176:179], v199 offset:56320
	global_load_lds_dwordx4 v[194:195], off
	v_lshl_add_u64 v[194:195], v[238:239], 0, s[34:35]
	s_mov_b32 m0, s90
	s_nop 0
	global_load_lds_dwordx4 v[194:195], off
	s_barrier
	s_waitcnt lgkmcnt(0)
	s_setprio 1
	s_waitcnt lgkmcnt(0)
	v_mfma_f32_16x16x32_bf16 v[94:97], v[122:125], v[148:151], v[94:97]
	v_mfma_f32_16x16x32_bf16 v[90:93], v[138:141], v[148:151], v[90:93]
	v_mfma_f32_16x16x32_bf16 v[86:89], v[122:125], v[156:159], v[86:89]
	v_mfma_f32_16x16x32_bf16 v[82:85], v[138:141], v[156:159], v[82:85]
	v_mfma_f32_16x16x32_bf16 v[78:81], v[122:125], v[164:167], v[78:81]
	v_mfma_f32_16x16x32_bf16 v[74:77], v[138:141], v[164:167], v[74:77]
	v_mfma_f32_16x16x32_bf16 v[70:73], v[122:125], v[172:175], v[70:73]
	v_mfma_f32_16x16x32_bf16 v[66:69], v[138:141], v[172:175], v[66:69]
	v_mfma_f32_16x16x32_bf16 v[94:97], v[126:129], v[152:155], v[94:97]
	v_mfma_f32_16x16x32_bf16 v[90:93], v[142:145], v[152:155], v[90:93]
	v_mfma_f32_16x16x32_bf16 v[86:89], v[126:129], v[160:163], v[86:89]
	v_mfma_f32_16x16x32_bf16 v[82:85], v[142:145], v[160:163], v[82:85]
	v_mfma_f32_16x16x32_bf16 v[78:81], v[126:129], v[168:171], v[78:81]
	v_mfma_f32_16x16x32_bf16 v[74:77], v[142:145], v[168:171], v[74:77]
	v_mfma_f32_16x16x32_bf16 v[70:73], v[126:129], v[176:179], v[70:73]
	v_mfma_f32_16x16x32_bf16 v[66:69], v[142:145], v[176:179], v[66:69]
	s_setprio 0
	s_barrier
	s_add_u32 s8, s8, 0x40080
	s_addc_u32 s9, s9, 0
	s_add_i32 s18, s18, s80
	s_mov_b32 m0, s18
	s_nop 0
	global_load_lds_dwordx4 v146, s[8:9]
	s_add_i32 m0, s18, 0x2000
	s_nop 0
	global_load_lds_dwordx4 v188, s[8:9]
	s_waitcnt vmcnt(6)
	s_mov_b32 s100, 0
	s_barrier
	s_setprio 1
	v_mfma_f32_16x16x32_bf16 v[30:33], v[206:209], v[148:151], v[30:33]
	v_mfma_f32_16x16x32_bf16 v[26:29], v[214:217], v[148:151], v[26:29]
	v_mfma_f32_16x16x32_bf16 v[22:25], v[206:209], v[156:159], v[22:25]
	v_mfma_f32_16x16x32_bf16 v[18:21], v[214:217], v[156:159], v[18:21]
	v_mfma_f32_16x16x32_bf16 v[14:17], v[206:209], v[164:167], v[14:17]
	v_mfma_f32_16x16x32_bf16 v[10:13], v[214:217], v[164:167], v[10:13]
	v_mfma_f32_16x16x32_bf16 v[6:9], v[206:209], v[172:175], v[6:9]
	v_mfma_f32_16x16x32_bf16 v[2:5], v[214:217], v[172:175], v[2:5]
	v_mfma_f32_16x16x32_bf16 v[30:33], v[210:213], v[152:155], v[30:33]
	v_mfma_f32_16x16x32_bf16 v[26:29], v[218:221], v[152:155], v[26:29]
	v_mfma_f32_16x16x32_bf16 v[22:25], v[210:213], v[160:163], v[22:25]
	v_mfma_f32_16x16x32_bf16 v[18:21], v[218:221], v[160:163], v[18:21]
	v_mfma_f32_16x16x32_bf16 v[14:17], v[210:213], v[168:171], v[14:17]
	v_mfma_f32_16x16x32_bf16 v[10:13], v[218:221], v[168:171], v[10:13]
	v_mfma_f32_16x16x32_bf16 v[6:9], v[210:213], v[176:179], v[6:9]
	v_mfma_f32_16x16x32_bf16 v[2:5], v[218:221], v[176:179], v[2:5]
	s_setprio 0
	s_add_i32 s24, s24, 2
	s_add_u32 s28, s28, 0x100
	s_addc_u32 s29, s29, 0
	s_add_u32 s22, s22, 0x100
	s_addc_u32 s23, s23, 0
	s_cmp_gt_u32 s24, 13
	s_barrier
	s_cbranch_scc1 .LBB0_1800

; __device__ __forceinline__ unsigned cvt_pk_bf16(float lo, float hi) { unsigned r; asm volatile("v_cvt_pk_bf16_f32 %0, %1, %2" : "=v"(r) : "v"(lo), "v"(hi)); return r; }
;     __device__ __forceinline__ bf16_t* act() const { return (bf16_t*)(ws + WS_PROJ); }
;     __device__ __forceinline__ void operator()(const AccT& acc, const gm::GUnit& u, int wr, int wc, int fr, int fq) const {
;     ...
;         if (u.sub < 8) {
;             bf16_t* at = (bf16_t*)(act + u.aux);
;             f32x4 bgs[2], bus[2];
; #pragma unroll
;             for (int bj = 0; bj < 2; ++bj) { const int col = u.pn * 128 + bj * 64 + wc * 16 + 4 * fq; bgs[bj] = *(const f32x4*)(bgate + u.e * 1024 + col); bus[bj] = *(const f32x4*)(bup + u.e * 1024 + col); }
;             __builtin_amdgcn_sched_barrier(0);
; #pragma unroll
;             for (int bj = 0; bj < 2; ++bj) {
;                 const int col = u.pn * 128 + bj * 64 + wc * 16 + 4 * fq;
;                 const f32x4 bgv = bgs[bj], buv = bus[bj];
; #pragma unroll
;                 for (int ai = 0; ai < 2; ++ai)
; #pragma unroll
;                     for (int m = 0; m < 4; ++m) {
;                         const int row = ai * 128 + wr * 64 + m * 16 + fr;
;                         f32x4 a4 = acc[ai][bj][m][0] + bgv, u4 = acc[ai][bj][m][1] + buv;
; #pragma unroll
;                         for (int j = 0; j < 4; ++j) { a4[j] = fminf(a4[j], 7.f); u4[j] = fminf(fmaxf(u4[j], -7.f), 7.f); }
;                         f32x4 e4 = a4 * (-1.702f * 1.4426950408889634f);
; #pragma unroll
;                         for (int j = 0; j < 4; ++j) e4[j] = __builtin_amdgcn_exp2f(e4[j]);
;                         e4 = e4 + 1.f;
; #pragma unroll
;                         for (int j = 0; j < 4; ++j) e4[j] = __builtin_amdgcn_rcpf(e4[j]);
;                         const f32x4 g4 = a4 * e4, o = g4 * u4 + g4;
;                         u32x2 w; w.x = cvt_pk_bf16(o[0], o[1]); w.y = cvt_pk_bf16(o[2], o[3]);
;                         *(u32x2*)(at + (size_t)row * DM + col) = w;
;                     }
.LBB0_1811:
	s_mov_b32 s100, 0
	s_mov_b64 s[8:9], 0
.LBB0_1812:
	s_and_b64 vcc, exec, s[8:9]
	s_cbranch_vccz .LBB0_1778
	s_lshl_b32 s8, s62, 10
	s_lshl_b32 s2, s2, 7
	s_ashr_i32 s9, s8, 31
	s_or_b32 s2, s2, s91
	s_lshl_b64 s[8:9], s[8:9], 2
	s_add_u32 s18, s67, s8
	v_lshl_add_u32 v154, v155, 2, s2
	s_addc_u32 s19, s68, s9
	s_add_u32 s8, s69, s8
	v_ashrrev_i32_e32 v155, 31, v154
	s_addc_u32 s9, s70, s9
	v_lshlrev_b64 v[122:123], 2, v[154:155]
	v_lshl_add_u64 v[124:125], s[18:19], 0, v[122:123]
	v_lshl_add_u64 v[122:123], s[8:9], 0, v[122:123]
	global_load_dwordx4 v[138:141], v[124:125], off
	global_load_dwordx4 v[126:129], v[124:125], off offset:256
	global_load_dwordx4 v[142:145], v[122:123], off
	s_nop 0
	global_load_dwordx4 v[122:125], v[122:123], off offset:256
	v_add_u32_e32 v148, 64, v154
	s_add_u32 s18, s63, s93
	v_ashrrev_i32_e32 v149, 31, v148
	s_addc_u32 s19, s71, 0
	s_waitcnt vmcnt(0)
	v_pk_add_f32 v[134:135], v[134:135], v[138:139]
	v_pk_add_f32 v[136:137], v[136:137], v[140:141]
	v_min_f32_e32 v134, 0x40e00000, v134
	v_min_f32_e32 v135, 0x40e00000, v135
	v_min_f32_e32 v136, 0x40e00000, v136
	v_min_f32_e32 v137, 0x40e00000, v137
	v_pk_mul_f32 v[156:157], v[134:135], s[12:13] op_sel_hi:[1,0]
	v_add_u32_e32 v152, s87, v151
	v_lshl_add_u64 v[150:151], v[154:155], 1, s[18:19]
	v_pk_mul_f32 v[154:155], v[136:137], s[12:13] op_sel_hi:[1,0]
	v_exp_f32_e32 v156, v156
	v_exp_f32_e32 v157, v157
	v_exp_f32_e32 v154, v154
	v_exp_f32_e32 v155, v155
	v_pk_add_f32 v[130:131], v[130:131], v[142:143]
	v_pk_add_f32 v[156:157], v[156:157], 1.0 op_sel_hi:[1,0]
	v_pk_add_f32 v[132:133], v[132:133], v[144:145]
	v_pk_add_f32 v[154:155], v[154:155], 1.0 op_sel_hi:[1,0]
	v_rcp_f32_e32 v156, v156
	v_rcp_f32_e32 v157, v157
	v_rcp_f32_e32 v154, v154
	v_rcp_f32_e32 v155, v155
	v_med3_f32 v130, v130, s21, v230
	v_med3_f32 v131, v131, s21, v230
	v_pk_mul_f32 v[134:135], v[134:135], v[156:157]
	v_med3_f32 v132, v132, s21, v230
	v_med3_f32 v133, v133, s21, v230
	v_pk_mul_f32 v[136:137], v[136:137], v[154:155]
	v_pk_fma_f32 v[130:131], v[130:131], v[134:135], v[134:135]
	v_ashrrev_i32_e32 v153, 31, v152
	v_pk_fma_f32 v[132:133], v[132:133], v[136:137], v[136:137]
	v_cvt_pk_bf16_f32 v134, v130, v131
	v_lshlrev_b64 v[130:131], 11, v[152:153]
	v_pk_add_f32 v[118:119], v[118:119], v[138:139]
	v_cvt_pk_bf16_f32 v135, v132, v133
	v_lshl_add_u64 v[132:133], v[150:151], 0, v[130:131]
	v_pk_add_f32 v[120:121], v[120:121], v[140:141]
	v_min_f32_e32 v118, 0x40e00000, v118
	v_min_f32_e32 v119, 0x40e00000, v119
	global_store_dwordx2 v[132:133], v[134:135], off
	v_min_f32_e32 v120, 0x40e00000, v120
	v_min_f32_e32 v121, 0x40e00000, v121
	v_pk_mul_f32 v[134:135], v[118:119], s[12:13] op_sel_hi:[1,0]
	v_pk_mul_f32 v[132:133], v[120:121], s[12:13] op_sel_hi:[1,0]
	v_exp_f32_e32 v134, v134
	v_exp_f32_e32 v135, v135
	v_exp_f32_e32 v132, v132
	v_exp_f32_e32 v133, v133
	v_pk_add_f32 v[114:115], v[114:115], v[142:143]
	v_pk_add_f32 v[134:135], v[134:135], 1.0 op_sel_hi:[1,0]
	v_pk_add_f32 v[116:117], v[116:117], v[144:145]
	v_pk_add_f32 v[132:133], v[132:133], 1.0 op_sel_hi:[1,0]
	v_rcp_f32_e32 v134, v134
	v_rcp_f32_e32 v135, v135
	v_rcp_f32_e32 v132, v132
	v_rcp_f32_e32 v133, v133
	v_med3_f32 v114, v114, s21, v230
	v_med3_f32 v115, v115, s21, v230
	v_add_u32_e32 v136, 16, v152
	v_pk_mul_f32 v[118:119], v[118:119], v[134:135]
	v_med3_f32 v116, v116, s21, v230
	v_med3_f32 v117, v117, s21, v230
	v_pk_mul_f32 v[120:121], v[120:121], v[132:133]
	v_pk_fma_f32 v[114:115], v[114:115], v[118:119], v[118:119]
	v_ashrrev_i32_e32 v137, 31, v136
	v_pk_fma_f32 v[116:117], v[116:117], v[120:121], v[120:121]
	v_cvt_pk_bf16_f32 v118, v114, v115
	v_lshlrev_b64 v[114:115], 11, v[136:137]
	v_pk_add_f32 v[110:111], v[110:111], v[138:139]
	v_cvt_pk_bf16_f32 v119, v116, v117
	v_lshl_add_u64 v[116:117], v[150:151], 0, v[114:115]
	v_pk_add_f32 v[112:113], v[112:113], v[140:141]
	v_min_f32_e32 v110, 0x40e00000, v110
	v_min_f32_e32 v111, 0x40e00000, v111
	global_store_dwordx2 v[116:117], v[118:119], off
	v_min_f32_e32 v112, 0x40e00000, v112
	v_min_f32_e32 v113, 0x40e00000, v113
	v_pk_mul_f32 v[118:119], v[110:111], s[12:13] op_sel_hi:[1,0]
	v_pk_mul_f32 v[116:117], v[112:113], s[12:13] op_sel_hi:[1,0]
	v_exp_f32_e32 v118, v118
	v_exp_f32_e32 v119, v119
	v_exp_f32_e32 v116, v116
	v_exp_f32_e32 v117, v117
	v_pk_add_f32 v[106:107], v[106:107], v[142:143]
	v_pk_add_f32 v[118:119], v[118:119], 1.0 op_sel_hi:[1,0]
	v_pk_add_f32 v[108:109], v[108:109], v[144:145]
	v_pk_add_f32 v[116:117], v[116:117], 1.0 op_sel_hi:[1,0]
	v_rcp_f32_e32 v118, v118
	v_rcp_f32_e32 v119, v119
	v_rcp_f32_e32 v116, v116
	v_rcp_f32_e32 v117, v117
	v_med3_f32 v106, v106, s21, v230
	v_med3_f32 v107, v107, s21, v230
	v_add_u32_e32 v120, 32, v152
	v_pk_mul_f32 v[110:111], v[110:111], v[118:119]
	v_med3_f32 v108, v108, s21, v230
	v_med3_f32 v109, v109, s21, v230
	v_pk_mul_f32 v[112:113], v[112:113], v[116:117]
	v_pk_fma_f32 v[106:107], v[106:107], v[110:111], v[110:111]
	v_ashrrev_i32_e32 v121, 31, v120
	v_pk_fma_f32 v[108:109], v[108:109], v[112:113], v[112:113]
	v_cvt_pk_bf16_f32 v110, v106, v107
	v_lshlrev_b64 v[106:107], 11, v[120:121]
	v_pk_add_f32 v[102:103], v[102:103], v[138:139]
	v_cvt_pk_bf16_f32 v111, v108, v109
	v_lshl_add_u64 v[108:109], v[150:151], 0, v[106:107]
	v_pk_add_f32 v[104:105], v[104:105], v[140:141]
	v_min_f32_e32 v102, 0x40e00000, v102
	v_min_f32_e32 v103, 0x40e00000, v103
	global_store_dwordx2 v[108:109], v[110:111], off
	v_min_f32_e32 v104, 0x40e00000, v104
	v_min_f32_e32 v105, 0x40e00000, v105
	v_pk_mul_f32 v[110:111], v[102:103], s[12:13] op_sel_hi:[1,0]
	v_pk_mul_f32 v[108:109], v[104:105], s[12:13] op_sel_hi:[1,0]
; __device__ __forceinline__ unsigned cvt_pk_bf16(float lo, float hi) { unsigned r; asm volatile("v_cvt_pk_bf16_f32 %0, %1, %2" : "=v"(r) : "v"(lo), "v"(hi)); return r; }
;     __device__ __forceinline__ bf16_t* act() const { return (bf16_t*)(ws + WS_PROJ); }
;     __device__ __forceinline__ void operator()(const AccT& acc, const gm::GUnit& u, int wr, int wc, int fr, int fq) const {
;     ...
;         if (u.sub < 8) {
;             bf16_t* at = (bf16_t*)(act + u.aux);
;             f32x4 bgs[2], bus[2];
; #pragma unroll
;             for (int bj = 0; bj < 2; ++bj) { const int col = u.pn * 128 + bj * 64 + wc * 16 + 4 * fq; bgs[bj] = *(const f32x4*)(bgate + u.e * 1024 + col); bus[bj] = *(const f32x4*)(bup + u.e * 1024 + col); }
;             __builtin_amdgcn_sched_barrier(0);
; #pragma unroll
;             for (int bj = 0; bj < 2; ++bj) {
;                 const int col = u.pn * 128 + bj * 64 + wc * 16 + 4 * fq;
;                 const f32x4 bgv = bgs[bj], buv = bus[bj];
; #pragma unroll
;                 for (int ai = 0; ai < 2; ++ai)
; #pragma unroll
;                     for (int m = 0; m < 4; ++m) {
;                         const int row = ai * 128 + wr * 64 + m * 16 + fr;
;                         f32x4 a4 = acc[ai][bj][m][0] + bgv, u4 = acc[ai][bj][m][1] + buv;
; #pragma unroll
;                         for (int j = 0; j < 4; ++j) { a4[j] = fminf(a4[j], 7.f); u4[j] = fminf(fmaxf(u4[j], -7.f), 7.f); }
;                         f32x4 e4 = a4 * (-1.702f * 1.4426950408889634f);
; #pragma unroll
;                         for (int j = 0; j < 4; ++j) e4[j] = __builtin_amdgcn_exp2f(e4[j]);
;                         e4 = e4 + 1.f;
; #pragma unroll
;                         for (int j = 0; j < 4; ++j) e4[j] = __builtin_amdgcn_rcpf(e4[j]);
;                         const f32x4 g4 = a4 * e4, o = g4 * u4 + g4;
;                         u32x2 w; w.x = cvt_pk_bf16(o[0], o[1]); w.y = cvt_pk_bf16(o[2], o[3]);
;                         *(u32x2*)(at + (size_t)row * DM + col) = w;
;                     }
	v_exp_f32_e32 v110, v110
	v_exp_f32_e32 v111, v111
	v_exp_f32_e32 v108, v108
	v_exp_f32_e32 v109, v109
	v_pk_add_f32 v[98:99], v[98:99], v[142:143]
	v_pk_add_f32 v[110:111], v[110:111], 1.0 op_sel_hi:[1,0]
	v_pk_add_f32 v[100:101], v[100:101], v[144:145]
	v_pk_add_f32 v[108:109], v[108:109], 1.0 op_sel_hi:[1,0]
	v_rcp_f32_e32 v110, v110
	v_rcp_f32_e32 v111, v111
	v_rcp_f32_e32 v108, v108
	v_rcp_f32_e32 v109, v109
	v_med3_f32 v98, v98, s21, v230
	v_med3_f32 v99, v99, s21, v230
	v_add_u32_e32 v112, 48, v152
	v_pk_mul_f32 v[102:103], v[102:103], v[110:111]
	v_med3_f32 v100, v100, s21, v230
	v_med3_f32 v101, v101, s21, v230
	v_pk_mul_f32 v[104:105], v[104:105], v[108:109]
	v_pk_fma_f32 v[98:99], v[98:99], v[102:103], v[102:103]
	v_ashrrev_i32_e32 v113, 31, v112
	v_pk_add_f32 v[94:95], v[94:95], v[138:139]
	v_pk_fma_f32 v[100:101], v[100:101], v[104:105], v[104:105]
	v_cvt_pk_bf16_f32 v102, v98, v99
	v_lshlrev_b64 v[98:99], 11, v[112:113]
	v_pk_add_f32 v[96:97], v[96:97], v[140:141]
	v_min_f32_e32 v94, 0x40e00000, v94
	v_min_f32_e32 v95, 0x40e00000, v95
	v_cvt_pk_bf16_f32 v103, v100, v101
	v_lshl_add_u64 v[100:101], v[150:151], 0, v[98:99]
	v_min_f32_e32 v96, 0x40e00000, v96
	v_min_f32_e32 v97, 0x40e00000, v97
	v_pk_mul_f32 v[104:105], v[94:95], s[12:13] op_sel_hi:[1,0]
	global_store_dwordx2 v[100:101], v[102:103], off
	v_pk_mul_f32 v[102:103], v[96:97], s[12:13] op_sel_hi:[1,0]
	v_exp_f32_e32 v104, v104
	v_exp_f32_e32 v105, v105
	v_exp_f32_e32 v102, v102
	v_exp_f32_e32 v103, v103
	v_pk_add_f32 v[90:91], v[90:91], v[142:143]
	v_pk_add_f32 v[104:105], v[104:105], 1.0 op_sel_hi:[1,0]
	v_add_u32_e32 v100, 0x80, v152
	v_pk_add_f32 v[102:103], v[102:103], 1.0 op_sel_hi:[1,0]
	v_rcp_f32_e32 v104, v104
	v_rcp_f32_e32 v105, v105
	v_rcp_f32_e32 v102, v102
	v_rcp_f32_e32 v103, v103
	v_pk_add_f32 v[92:93], v[92:93], v[144:145]
	v_med3_f32 v90, v90, s21, v230
	v_med3_f32 v91, v91, s21, v230
	v_pk_mul_f32 v[94:95], v[94:95], v[104:105]
	v_med3_f32 v92, v92, s21, v230
	v_med3_f32 v93, v93, s21, v230
	v_pk_mul_f32 v[96:97], v[96:97], v[102:103]
	v_pk_fma_f32 v[90:91], v[90:91], v[94:95], v[94:95]
	v_ashrrev_i32_e32 v101, 31, v100
	v_pk_fma_f32 v[92:93], v[92:93], v[96:97], v[96:97]
	v_cvt_pk_bf16_f32 v94, v90, v91
	v_lshlrev_b64 v[90:91], 11, v[100:101]
	v_pk_add_f32 v[86:87], v[86:87], v[138:139]
	v_cvt_pk_bf16_f32 v95, v92, v93
	v_lshl_add_u64 v[92:93], v[150:151], 0, v[90:91]
	v_pk_add_f32 v[88:89], v[88:89], v[140:141]
	v_min_f32_e32 v86, 0x40e00000, v86
	v_min_f32_e32 v87, 0x40e00000, v87
	global_store_dwordx2 v[92:93], v[94:95], off
	v_min_f32_e32 v88, 0x40e00000, v88
	v_min_f32_e32 v89, 0x40e00000, v89
	v_pk_mul_f32 v[94:95], v[86:87], s[12:13] op_sel_hi:[1,0]
	v_pk_mul_f32 v[92:93], v[88:89], s[12:13] op_sel_hi:[1,0]
	v_exp_f32_e32 v94, v94
	v_exp_f32_e32 v95, v95
	v_exp_f32_e32 v92, v92
	v_exp_f32_e32 v93, v93
	v_pk_add_f32 v[82:83], v[82:83], v[142:143]
	v_pk_add_f32 v[94:95], v[94:95], 1.0 op_sel_hi:[1,0]
	v_pk_add_f32 v[84:85], v[84:85], v[144:145]
	v_pk_add_f32 v[92:93], v[92:93], 1.0 op_sel_hi:[1,0]
	v_rcp_f32_e32 v94, v94
	v_rcp_f32_e32 v95, v95
	v_rcp_f32_e32 v92, v92
	v_rcp_f32_e32 v93, v93
	v_med3_f32 v82, v82, s21, v230
	v_med3_f32 v83, v83, s21, v230
	v_add_u32_e32 v96, 0x90, v152
	v_pk_mul_f32 v[86:87], v[86:87], v[94:95]
	v_med3_f32 v84, v84, s21, v230
	v_med3_f32 v85, v85, s21, v230
	v_pk_mul_f32 v[88:89], v[88:89], v[92:93]
	v_pk_fma_f32 v[82:83], v[82:83], v[86:87], v[86:87]
	v_ashrrev_i32_e32 v97, 31, v96
	v_pk_fma_f32 v[84:85], v[84:85], v[88:89], v[88:89]
	v_cvt_pk_bf16_f32 v86, v82, v83
	v_lshlrev_b64 v[82:83], 11, v[96:97]
	v_pk_add_f32 v[78:79], v[78:79], v[138:139]
	v_cvt_pk_bf16_f32 v87, v84, v85
	v_lshl_add_u64 v[84:85], v[150:151], 0, v[82:83]
	v_pk_add_f32 v[80:81], v[80:81], v[140:141]
	v_min_f32_e32 v78, 0x40e00000, v78
	v_min_f32_e32 v79, 0x40e00000, v79
	global_store_dwordx2 v[84:85], v[86:87], off
	v_min_f32_e32 v80, 0x40e00000, v80
	v_min_f32_e32 v81, 0x40e00000, v81
	v_pk_mul_f32 v[86:87], v[78:79], s[12:13] op_sel_hi:[1,0]
	v_pk_mul_f32 v[84:85], v[80:81], s[12:13] op_sel_hi:[1,0]
	v_exp_f32_e32 v86, v86
	v_exp_f32_e32 v87, v87
	v_exp_f32_e32 v84, v84
	v_exp_f32_e32 v85, v85
	v_pk_add_f32 v[74:75], v[74:75], v[142:143]
	v_pk_add_f32 v[86:87], v[86:87], 1.0 op_sel_hi:[1,0]
	v_pk_add_f32 v[76:77], v[76:77], v[144:145]
	v_pk_add_f32 v[84:85], v[84:85], 1.0 op_sel_hi:[1,0]
	v_rcp_f32_e32 v86, v86
	v_rcp_f32_e32 v87, v87
	v_rcp_f32_e32 v84, v84
	v_rcp_f32_e32 v85, v85
	v_med3_f32 v74, v74, s21, v230
	v_med3_f32 v75, v75, s21, v230
	v_add_u32_e32 v88, 0xa0, v152
	v_pk_mul_f32 v[78:79], v[78:79], v[86:87]
	v_med3_f32 v76, v76, s21, v230
	v_med3_f32 v77, v77, s21, v230
	v_pk_mul_f32 v[80:81], v[80:81], v[84:85]
	v_pk_fma_f32 v[74:75], v[74:75], v[78:79], v[78:79]
	v_ashrrev_i32_e32 v89, 31, v88
	v_pk_fma_f32 v[76:77], v[76:77], v[80:81], v[80:81]
	v_cvt_pk_bf16_f32 v78, v74, v75
	v_lshlrev_b64 v[74:75], 11, v[88:89]
	v_pk_add_f32 v[70:71], v[70:71], v[138:139]
	v_cvt_pk_bf16_f32 v79, v76, v77
	v_lshl_add_u64 v[76:77], v[150:151], 0, v[74:75]
	v_pk_add_f32 v[72:73], v[72:73], v[140:141]
	v_min_f32_e32 v70, 0x40e00000, v70
	v_min_f32_e32 v71, 0x40e00000, v71
	global_store_dwordx2 v[76:77], v[78:79], off
	v_min_f32_e32 v72, 0x40e00000, v72
	v_min_f32_e32 v73, 0x40e00000, v73
	v_pk_mul_f32 v[78:79], v[70:71], s[12:13] op_sel_hi:[1,0]
	v_pk_mul_f32 v[76:77], v[72:73], s[12:13] op_sel_hi:[1,0]
	v_exp_f32_e32 v78, v78
	v_exp_f32_e32 v79, v79
	v_exp_f32_e32 v76, v76
	v_exp_f32_e32 v77, v77
	v_pk_add_f32 v[66:67], v[66:67], v[142:143]
	v_pk_add_f32 v[78:79], v[78:79], 1.0 op_sel_hi:[1,0]
	v_pk_add_f32 v[68:69], v[68:69], v[144:145]
; __device__ __forceinline__ unsigned cvt_pk_bf16(float lo, float hi) { unsigned r; asm volatile("v_cvt_pk_bf16_f32 %0, %1, %2" : "=v"(r) : "v"(lo), "v"(hi)); return r; }
;     __device__ __forceinline__ bf16_t* act() const { return (bf16_t*)(ws + WS_PROJ); }
;     __device__ __forceinline__ void operator()(const AccT& acc, const gm::GUnit& u, int wr, int wc, int fr, int fq) const {
;     ...
;         if (u.sub < 8) {
;             bf16_t* at = (bf16_t*)(act + u.aux);
;             f32x4 bgs[2], bus[2];
; #pragma unroll
;             for (int bj = 0; bj < 2; ++bj) { const int col = u.pn * 128 + bj * 64 + wc * 16 + 4 * fq; bgs[bj] = *(const f32x4*)(bgate + u.e * 1024 + col); bus[bj] = *(const f32x4*)(bup + u.e * 1024 + col); }
;             __builtin_amdgcn_sched_barrier(0);
; #pragma unroll
;             for (int bj = 0; bj < 2; ++bj) {
;                 const int col = u.pn * 128 + bj * 64 + wc * 16 + 4 * fq;
;                 const f32x4 bgv = bgs[bj], buv = bus[bj];
; #pragma unroll
;                 for (int ai = 0; ai < 2; ++ai)
; #pragma unroll
;                     for (int m = 0; m < 4; ++m) {
;                         const int row = ai * 128 + wr * 64 + m * 16 + fr;
;                         f32x4 a4 = acc[ai][bj][m][0] + bgv, u4 = acc[ai][bj][m][1] + buv;
; #pragma unroll
;                         for (int j = 0; j < 4; ++j) { a4[j] = fminf(a4[j], 7.f); u4[j] = fminf(fmaxf(u4[j], -7.f), 7.f); }
;                         f32x4 e4 = a4 * (-1.702f * 1.4426950408889634f);
; #pragma unroll
;                         for (int j = 0; j < 4; ++j) e4[j] = __builtin_amdgcn_exp2f(e4[j]);
;                         e4 = e4 + 1.f;
; #pragma unroll
;                         for (int j = 0; j < 4; ++j) e4[j] = __builtin_amdgcn_rcpf(e4[j]);
;                         const f32x4 g4 = a4 * e4, o = g4 * u4 + g4;
;                         u32x2 w; w.x = cvt_pk_bf16(o[0], o[1]); w.y = cvt_pk_bf16(o[2], o[3]);
;                         *(u32x2*)(at + (size_t)row * DM + col) = w;
;                     }
	v_pk_add_f32 v[76:77], v[76:77], 1.0 op_sel_hi:[1,0]
	v_rcp_f32_e32 v78, v78
	v_rcp_f32_e32 v79, v79
	v_rcp_f32_e32 v76, v76
	v_rcp_f32_e32 v77, v77
	v_med3_f32 v66, v66, s21, v230
	v_med3_f32 v67, v67, s21, v230
	v_add_u32_e32 v80, 0xb0, v152
	v_pk_mul_f32 v[70:71], v[70:71], v[78:79]
	v_med3_f32 v68, v68, s21, v230
	v_med3_f32 v69, v69, s21, v230
	v_pk_mul_f32 v[72:73], v[72:73], v[76:77]
	v_pk_fma_f32 v[66:67], v[66:67], v[70:71], v[70:71]
	v_ashrrev_i32_e32 v81, 31, v80
	v_pk_fma_f32 v[68:69], v[68:69], v[72:73], v[72:73]
	v_cvt_pk_bf16_f32 v70, v66, v67
	v_lshlrev_b64 v[66:67], 11, v[80:81]
	v_pk_add_f32 v[64:65], v[64:65], v[128:129]
	v_pk_add_f32 v[62:63], v[62:63], v[126:127]
	v_cvt_pk_bf16_f32 v71, v68, v69
	v_lshl_add_u64 v[68:69], v[150:151], 0, v[66:67]
	v_min_f32_e32 v62, 0x40e00000, v62
	v_min_f32_e32 v63, 0x40e00000, v63
	v_min_f32_e32 v64, 0x40e00000, v64
	v_min_f32_e32 v65, 0x40e00000, v65
	global_store_dwordx2 v[68:69], v[70:71], off
	v_pk_mul_f32 v[70:71], v[64:65], s[12:13] op_sel_hi:[1,0]
	v_pk_mul_f32 v[72:73], v[62:63], s[12:13] op_sel_hi:[1,0]
	v_exp_f32_e32 v70, v70
	v_exp_f32_e32 v72, v72
	v_exp_f32_e32 v73, v73
	v_exp_f32_e32 v71, v71
	v_pk_add_f32 v[60:61], v[60:61], v[124:125]
	v_pk_add_f32 v[58:59], v[58:59], v[122:123]
	v_pk_add_f32 v[72:73], v[72:73], 1.0 op_sel_hi:[1,0]
	v_pk_add_f32 v[70:71], v[70:71], 1.0 op_sel_hi:[1,0]
	v_rcp_f32_e32 v72, v72
	v_rcp_f32_e32 v73, v73
	v_rcp_f32_e32 v70, v70
	v_rcp_f32_e32 v71, v71
	v_med3_f32 v58, v58, s21, v230
	v_med3_f32 v59, v59, s21, v230
	v_med3_f32 v60, v60, s21, v230
	v_med3_f32 v61, v61, s21, v230
	v_pk_mul_f32 v[64:65], v[64:65], v[70:71]
	v_pk_mul_f32 v[62:63], v[62:63], v[72:73]
	v_lshl_add_u64 v[68:69], v[148:149], 1, s[18:19]
	v_pk_fma_f32 v[60:61], v[60:61], v[64:65], v[64:65]
	v_pk_fma_f32 v[58:59], v[58:59], v[62:63], v[62:63]
	v_pk_add_f32 v[56:57], v[56:57], v[128:129]
	v_pk_add_f32 v[54:55], v[54:55], v[126:127]
	v_cvt_pk_bf16_f32 v58, v58, v59
	v_cvt_pk_bf16_f32 v59, v60, v61
	v_lshl_add_u64 v[60:61], v[68:69], 0, v[130:131]
	v_min_f32_e32 v54, 0x40e00000, v54
	v_min_f32_e32 v55, 0x40e00000, v55
	v_min_f32_e32 v56, 0x40e00000, v56
	v_min_f32_e32 v57, 0x40e00000, v57
	global_store_dwordx2 v[60:61], v[58:59], off
	v_pk_mul_f32 v[58:59], v[56:57], s[12:13] op_sel_hi:[1,0]
	v_pk_mul_f32 v[60:61], v[54:55], s[12:13] op_sel_hi:[1,0]
	v_exp_f32_e32 v58, v58
	v_exp_f32_e32 v60, v60
	v_exp_f32_e32 v61, v61
	v_exp_f32_e32 v59, v59
	v_pk_add_f32 v[52:53], v[52:53], v[124:125]
	v_pk_add_f32 v[50:51], v[50:51], v[122:123]
	v_pk_add_f32 v[60:61], v[60:61], 1.0 op_sel_hi:[1,0]
	v_pk_add_f32 v[58:59], v[58:59], 1.0 op_sel_hi:[1,0]
	v_rcp_f32_e32 v60, v60
	v_rcp_f32_e32 v61, v61
	v_rcp_f32_e32 v58, v58
	v_rcp_f32_e32 v59, v59
	v_med3_f32 v50, v50, s21, v230
	v_med3_f32 v51, v51, s21, v230
	v_med3_f32 v52, v52, s21, v230
	v_med3_f32 v53, v53, s21, v230
	v_pk_mul_f32 v[56:57], v[56:57], v[58:59]
	v_pk_mul_f32 v[54:55], v[54:55], v[60:61]
	v_pk_fma_f32 v[52:53], v[52:53], v[56:57], v[56:57]
	v_pk_fma_f32 v[50:51], v[50:51], v[54:55], v[54:55]
	v_pk_add_f32 v[48:49], v[48:49], v[128:129]
	v_pk_add_f32 v[46:47], v[46:47], v[126:127]
	v_cvt_pk_bf16_f32 v50, v50, v51
	v_cvt_pk_bf16_f32 v51, v52, v53
	v_lshl_add_u64 v[52:53], v[68:69], 0, v[114:115]
	v_min_f32_e32 v46, 0x40e00000, v46
	v_min_f32_e32 v47, 0x40e00000, v47
	v_min_f32_e32 v48, 0x40e00000, v48
	v_min_f32_e32 v49, 0x40e00000, v49
	global_store_dwordx2 v[52:53], v[50:51], off
	v_pk_mul_f32 v[50:51], v[48:49], s[12:13] op_sel_hi:[1,0]
	v_pk_mul_f32 v[52:53], v[46:47], s[12:13] op_sel_hi:[1,0]
	v_exp_f32_e32 v50, v50
	v_exp_f32_e32 v52, v52
	v_exp_f32_e32 v53, v53
	v_exp_f32_e32 v51, v51
	v_pk_add_f32 v[44:45], v[44:45], v[124:125]
	v_pk_add_f32 v[42:43], v[42:43], v[122:123]
	v_pk_add_f32 v[52:53], v[52:53], 1.0 op_sel_hi:[1,0]
	v_pk_add_f32 v[50:51], v[50:51], 1.0 op_sel_hi:[1,0]
	v_rcp_f32_e32 v52, v52
	v_rcp_f32_e32 v53, v53
	v_rcp_f32_e32 v50, v50
	v_rcp_f32_e32 v51, v51
	v_med3_f32 v42, v42, s21, v230
	v_med3_f32 v43, v43, s21, v230
	v_med3_f32 v44, v44, s21, v230
	v_med3_f32 v45, v45, s21, v230
	v_pk_mul_f32 v[48:49], v[48:49], v[50:51]
	v_pk_mul_f32 v[46:47], v[46:47], v[52:53]
	v_pk_fma_f32 v[44:45], v[44:45], v[48:49], v[48:49]
	v_pk_fma_f32 v[42:43], v[42:43], v[46:47], v[46:47]
	v_pk_add_f32 v[40:41], v[40:41], v[128:129]
	v_pk_add_f32 v[38:39], v[38:39], v[126:127]
	v_cvt_pk_bf16_f32 v42, v42, v43
	v_cvt_pk_bf16_f32 v43, v44, v45
	v_lshl_add_u64 v[44:45], v[68:69], 0, v[106:107]
	v_min_f32_e32 v38, 0x40e00000, v38
	v_min_f32_e32 v39, 0x40e00000, v39
	v_min_f32_e32 v40, 0x40e00000, v40
	v_min_f32_e32 v41, 0x40e00000, v41
	global_store_dwordx2 v[44:45], v[42:43], off
	v_pk_mul_f32 v[42:43], v[40:41], s[12:13] op_sel_hi:[1,0]
	v_pk_mul_f32 v[44:45], v[38:39], s[12:13] op_sel_hi:[1,0]
	v_exp_f32_e32 v42, v42
	v_exp_f32_e32 v44, v44
	v_exp_f32_e32 v45, v45
	v_exp_f32_e32 v43, v43
	v_pk_add_f32 v[36:37], v[36:37], v[124:125]
	v_pk_add_f32 v[34:35], v[34:35], v[122:123]
	v_pk_add_f32 v[44:45], v[44:45], 1.0 op_sel_hi:[1,0]
	v_pk_add_f32 v[42:43], v[42:43], 1.0 op_sel_hi:[1,0]
	v_rcp_f32_e32 v44, v44
	v_rcp_f32_e32 v45, v45
	v_rcp_f32_e32 v42, v42
	v_rcp_f32_e32 v43, v43
	v_med3_f32 v34, v34, s21, v230
	v_med3_f32 v35, v35, s21, v230
; __device__ __forceinline__ unsigned cvt_pk_bf16(float lo, float hi) { unsigned r; asm volatile("v_cvt_pk_bf16_f32 %0, %1, %2" : "=v"(r) : "v"(lo), "v"(hi)); return r; }
;     __device__ __forceinline__ bf16_t* act() const { return (bf16_t*)(ws + WS_PROJ); }
;     __device__ __forceinline__ void operator()(const AccT& acc, const gm::GUnit& u, int wr, int wc, int fr, int fq) const {
;     ...
;         if (u.sub < 8) {
;             bf16_t* at = (bf16_t*)(act + u.aux);
;             f32x4 bgs[2], bus[2];
; #pragma unroll
;             for (int bj = 0; bj < 2; ++bj) { const int col = u.pn * 128 + bj * 64 + wc * 16 + 4 * fq; bgs[bj] = *(const f32x4*)(bgate + u.e * 1024 + col); bus[bj] = *(const f32x4*)(bup + u.e * 1024 + col); }
;             __builtin_amdgcn_sched_barrier(0);
; #pragma unroll
;             for (int bj = 0; bj < 2; ++bj) {
;                 const int col = u.pn * 128 + bj * 64 + wc * 16 + 4 * fq;
;                 const f32x4 bgv = bgs[bj], buv = bus[bj];
; #pragma unroll
;                 for (int ai = 0; ai < 2; ++ai)
; #pragma unroll
;                     for (int m = 0; m < 4; ++m) {
;                         const int row = ai * 128 + wr * 64 + m * 16 + fr;
;                         f32x4 a4 = acc[ai][bj][m][0] + bgv, u4 = acc[ai][bj][m][1] + buv;
; #pragma unroll
;                         for (int j = 0; j < 4; ++j) { a4[j] = fminf(a4[j], 7.f); u4[j] = fminf(fmaxf(u4[j], -7.f), 7.f); }
;                         f32x4 e4 = a4 * (-1.702f * 1.4426950408889634f);
; #pragma unroll
;                         for (int j = 0; j < 4; ++j) e4[j] = __builtin_amdgcn_exp2f(e4[j]);
;                         e4 = e4 + 1.f;
; #pragma unroll
;                         for (int j = 0; j < 4; ++j) e4[j] = __builtin_amdgcn_rcpf(e4[j]);
;                         const f32x4 g4 = a4 * e4, o = g4 * u4 + g4;
;                         u32x2 w; w.x = cvt_pk_bf16(o[0], o[1]); w.y = cvt_pk_bf16(o[2], o[3]);
;                         *(u32x2*)(at + (size_t)row * DM + col) = w;
;                     }
	v_med3_f32 v36, v36, s21, v230
	v_med3_f32 v37, v37, s21, v230
	v_pk_mul_f32 v[40:41], v[40:41], v[42:43]
	v_pk_mul_f32 v[38:39], v[38:39], v[44:45]
	v_pk_fma_f32 v[36:37], v[36:37], v[40:41], v[40:41]
	v_pk_fma_f32 v[34:35], v[34:35], v[38:39], v[38:39]
	v_pk_add_f32 v[32:33], v[32:33], v[128:129]
	v_pk_add_f32 v[30:31], v[30:31], v[126:127]
	v_cvt_pk_bf16_f32 v34, v34, v35
	v_cvt_pk_bf16_f32 v35, v36, v37
	v_lshl_add_u64 v[36:37], v[68:69], 0, v[98:99]
	v_min_f32_e32 v30, 0x40e00000, v30
	v_min_f32_e32 v31, 0x40e00000, v31
	v_min_f32_e32 v32, 0x40e00000, v32
	v_min_f32_e32 v33, 0x40e00000, v33
	global_store_dwordx2 v[36:37], v[34:35], off
	v_pk_mul_f32 v[34:35], v[32:33], s[12:13] op_sel_hi:[1,0]
	v_pk_mul_f32 v[36:37], v[30:31], s[12:13] op_sel_hi:[1,0]
	v_exp_f32_e32 v34, v34
	v_exp_f32_e32 v36, v36
	v_exp_f32_e32 v37, v37
	v_exp_f32_e32 v35, v35
	v_pk_add_f32 v[28:29], v[28:29], v[124:125]
	v_pk_add_f32 v[26:27], v[26:27], v[122:123]
	v_pk_add_f32 v[36:37], v[36:37], 1.0 op_sel_hi:[1,0]
	v_pk_add_f32 v[34:35], v[34:35], 1.0 op_sel_hi:[1,0]
	v_rcp_f32_e32 v36, v36
	v_rcp_f32_e32 v37, v37
	v_rcp_f32_e32 v34, v34
	v_rcp_f32_e32 v35, v35
	v_med3_f32 v26, v26, s21, v230
	v_med3_f32 v27, v27, s21, v230
	v_med3_f32 v28, v28, s21, v230
	v_med3_f32 v29, v29, s21, v230
	v_pk_mul_f32 v[32:33], v[32:33], v[34:35]
	v_pk_mul_f32 v[30:31], v[30:31], v[36:37]
	v_pk_fma_f32 v[28:29], v[28:29], v[32:33], v[32:33]
	v_pk_fma_f32 v[26:27], v[26:27], v[30:31], v[30:31]
	v_pk_add_f32 v[24:25], v[24:25], v[128:129]
	v_pk_add_f32 v[22:23], v[22:23], v[126:127]
	v_cvt_pk_bf16_f32 v26, v26, v27
	v_cvt_pk_bf16_f32 v27, v28, v29
	v_lshl_add_u64 v[28:29], v[68:69], 0, v[90:91]
	v_min_f32_e32 v22, 0x40e00000, v22
	v_min_f32_e32 v23, 0x40e00000, v23
	v_min_f32_e32 v24, 0x40e00000, v24
	v_min_f32_e32 v25, 0x40e00000, v25
	global_store_dwordx2 v[28:29], v[26:27], off
	v_pk_mul_f32 v[26:27], v[24:25], s[12:13] op_sel_hi:[1,0]
	v_pk_mul_f32 v[28:29], v[22:23], s[12:13] op_sel_hi:[1,0]
	v_exp_f32_e32 v26, v26
	v_exp_f32_e32 v28, v28
	v_exp_f32_e32 v29, v29
	v_exp_f32_e32 v27, v27
	v_pk_add_f32 v[20:21], v[20:21], v[124:125]
	v_pk_add_f32 v[18:19], v[18:19], v[122:123]
	v_pk_add_f32 v[28:29], v[28:29], 1.0 op_sel_hi:[1,0]
	v_pk_add_f32 v[26:27], v[26:27], 1.0 op_sel_hi:[1,0]
	v_rcp_f32_e32 v28, v28
	v_rcp_f32_e32 v29, v29
	v_rcp_f32_e32 v26, v26
	v_rcp_f32_e32 v27, v27
	v_med3_f32 v18, v18, s21, v230
	v_med3_f32 v19, v19, s21, v230
	v_med3_f32 v20, v20, s21, v230
	v_med3_f32 v21, v21, s21, v230
	v_pk_mul_f32 v[24:25], v[24:25], v[26:27]
	v_pk_mul_f32 v[22:23], v[22:23], v[28:29]
	v_pk_fma_f32 v[20:21], v[20:21], v[24:25], v[24:25]
	v_pk_fma_f32 v[18:19], v[18:19], v[22:23], v[22:23]
	v_pk_add_f32 v[16:17], v[16:17], v[128:129]
	v_pk_add_f32 v[14:15], v[14:15], v[126:127]
	v_cvt_pk_bf16_f32 v18, v18, v19
	v_cvt_pk_bf16_f32 v19, v20, v21
	v_lshl_add_u64 v[20:21], v[68:69], 0, v[82:83]
	v_min_f32_e32 v14, 0x40e00000, v14
	v_min_f32_e32 v15, 0x40e00000, v15
	v_min_f32_e32 v16, 0x40e00000, v16
	v_min_f32_e32 v17, 0x40e00000, v17
	global_store_dwordx2 v[20:21], v[18:19], off
	v_pk_mul_f32 v[18:19], v[16:17], s[12:13] op_sel_hi:[1,0]
	v_pk_mul_f32 v[20:21], v[14:15], s[12:13] op_sel_hi:[1,0]
	v_exp_f32_e32 v18, v18
	v_exp_f32_e32 v20, v20
	v_exp_f32_e32 v21, v21
	v_exp_f32_e32 v19, v19
	v_pk_add_f32 v[12:13], v[12:13], v[124:125]
	v_pk_add_f32 v[10:11], v[10:11], v[122:123]
	v_pk_add_f32 v[20:21], v[20:21], 1.0 op_sel_hi:[1,0]
	v_pk_add_f32 v[18:19], v[18:19], 1.0 op_sel_hi:[1,0]
	v_rcp_f32_e32 v20, v20
	v_rcp_f32_e32 v21, v21
	v_rcp_f32_e32 v18, v18
	v_rcp_f32_e32 v19, v19
	v_med3_f32 v10, v10, s21, v230
	v_med3_f32 v11, v11, s21, v230
	v_med3_f32 v12, v12, s21, v230
	v_med3_f32 v13, v13, s21, v230
	v_pk_mul_f32 v[16:17], v[16:17], v[18:19]
	v_pk_mul_f32 v[14:15], v[14:15], v[20:21]
	v_pk_fma_f32 v[12:13], v[12:13], v[16:17], v[16:17]
	v_pk_fma_f32 v[10:11], v[10:11], v[14:15], v[14:15]
	v_pk_add_f32 v[8:9], v[8:9], v[128:129]
	v_pk_add_f32 v[6:7], v[6:7], v[126:127]
	v_cvt_pk_bf16_f32 v10, v10, v11
	v_cvt_pk_bf16_f32 v11, v12, v13
	v_lshl_add_u64 v[12:13], v[68:69], 0, v[74:75]
	v_min_f32_e32 v6, 0x40e00000, v6
	v_min_f32_e32 v7, 0x40e00000, v7
	v_min_f32_e32 v8, 0x40e00000, v8
	v_min_f32_e32 v9, 0x40e00000, v9
	global_store_dwordx2 v[12:13], v[10:11], off
	v_pk_mul_f32 v[10:11], v[8:9], s[12:13] op_sel_hi:[1,0]
	v_pk_mul_f32 v[12:13], v[6:7], s[12:13] op_sel_hi:[1,0]
	v_exp_f32_e32 v10, v10
	v_exp_f32_e32 v12, v12
	v_exp_f32_e32 v13, v13
	v_exp_f32_e32 v11, v11
	v_pk_add_f32 v[4:5], v[4:5], v[124:125]
	v_pk_add_f32 v[2:3], v[2:3], v[122:123]
	v_pk_add_f32 v[12:13], v[12:13], 1.0 op_sel_hi:[1,0]
	v_pk_add_f32 v[10:11], v[10:11], 1.0 op_sel_hi:[1,0]
	v_rcp_f32_e32 v12, v12
	v_rcp_f32_e32 v13, v13
	v_rcp_f32_e32 v10, v10
	v_rcp_f32_e32 v11, v11
	v_med3_f32 v2, v2, s21, v230
	v_med3_f32 v3, v3, s21, v230
	v_med3_f32 v4, v4, s21, v230
	v_med3_f32 v5, v5, s21, v230
	v_pk_mul_f32 v[8:9], v[8:9], v[10:11]
	v_pk_mul_f32 v[6:7], v[6:7], v[12:13]
	v_pk_fma_f32 v[4:5], v[4:5], v[8:9], v[8:9]
	v_pk_fma_f32 v[2:3], v[2:3], v[6:7], v[6:7]
	s_nop 0
	v_cvt_pk_bf16_f32 v2, v2, v3
	v_cvt_pk_bf16_f32 v3, v4, v5
	v_lshl_add_u64 v[4:5], v[68:69], 0, v[66:67]
	global_store_dwordx2 v[4:5], v[2:3], off
	s_mov_b32 s100, 1
	s_branch .LBB0_1778
